# attention tile loops: c1 QK MFMAs spaced between the exps of c0, first-half P.V MFMAs between the exps of the second half
# speedup vs baseline: 1.0059x; 1.0059x over previous
; __device__ __forceinline__ unsigned cvtpk(float lo, float hi) { f32x2_t v = {lo, hi}; bf16x2_t b = __builtin_convertvector(v, bf16x2_t); return __builtin_bit_cast(unsigned, b); }
; template <class BIAS>
; __device__ __forceinline__ void attn_tiles(char* shm, const UnitIO& io, int t_begin, int t_end, const BIAS& B, int tid) {
;     ...
;             for (int d0 = 0; d0 < 4; ++d0) { c0 = __builtin_amdgcn_mfma_f32_32x32x16_bf16(kf[2 * d0], qr[d0], c0, 0, 0, 0); c1 = __builtin_amdgcn_mfma_f32_32x32x16_bf16(kf[2 * d0 + 1], qr[d0], c1, 0, 0, 0); }
;             float s0 = 0.f;
; #pragma unroll
;             for (int r = 0; r < 16; ++r) c0[r] = __builtin_amdgcn_exp2f(c0[r]);
;             { f32x2_t s2 = (f32x2_t){c0[0], c0[1]};
; #pragma unroll
;               for (int i = 1; i < 8; ++i) s2 += (f32x2_t){c0[2 * i], c0[2 * i + 1]};
;               s0 = s2[0] + s2[1]; }
;             l_reg += s0;
; #pragma unroll
;             for (int i = 0; i < 4; ++i) { pw[0][i] = cvtpk(c0[2 * i], c0[2 * i + 1]); pw[1][i] = cvtpk(c0[8 + 2 * i], c0[9 + 2 * i]); }
;             c1x = c1;
.LBB0_303:
	s_waitcnt lgkmcnt(0)
	s_nop 0
	v_mfma_f32_32x32x16_bf16 v[50:65], v[98:101], v[66:69], v[50:65]
	v_mfma_f32_32x32x16_bf16 v[50:65], v[102:105], v[70:73], v[50:65]
	v_mfma_f32_32x32x16_bf16 v[50:65], v[106:109], v[74:77], v[50:65]
	v_mfma_f32_32x32x16_bf16 v[50:65], v[110:113], v[78:81], v[50:65]
	v_mfma_f32_32x32x16_bf16 v[34:49], v[94:97], v[66:69], v[34:49]
	s_nop 10
	v_exp_f32_e32 v50, v50
	v_exp_f32_e32 v51, v51
	v_exp_f32_e32 v52, v52
	v_exp_f32_e32 v53, v53
	v_mfma_f32_32x32x16_bf16 v[34:49], v[90:93], v[70:73], v[34:49]
	v_exp_f32_e32 v98, v54
	v_exp_f32_e32 v99, v55
	v_exp_f32_e32 v100, v56
	v_exp_f32_e32 v101, v57
	v_mfma_f32_32x32x16_bf16 v[34:49], v[86:89], v[74:77], v[34:49]
	v_exp_f32_e32 v54, v58
	v_exp_f32_e32 v55, v59
	v_exp_f32_e32 v56, v60
	v_exp_f32_e32 v57, v61
	v_mfma_f32_32x32x16_bf16 v[34:49], v[82:85], v[78:81], v[34:49]
	v_exp_f32_e32 v58, v62
	v_exp_f32_e32 v59, v63
	v_add_f32_e32 v62, v50, v52
	v_add_f32_e32 v63, v51, v53
	v_add_f32_e64 v62, v98, v62
	v_add_f32_e64 v63, v99, v63
	v_exp_f32_e32 v60, v64
	v_exp_f32_e32 v61, v65
	v_add_f32_e32 v62, v100, v62
	v_add_f32_e32 v63, v101, v63
	v_cvt_pk_bf16_f32 v50, v50, v51
	v_add_f32_e32 v62, v54, v62
	v_add_f32_e32 v63, v55, v63
	v_cvt_pk_bf16_f32 v54, v54, v55
	v_add_f32_e32 v62, v56, v62
	v_add_f32_e32 v63, v57, v63
	v_cvt_pk_bf16_f32 v51, v52, v53
	v_add_f32_e32 v62, v58, v62
	v_add_f32_e32 v63, v59, v63
	v_cvt_pk_bf16_f32 v55, v56, v57
	v_add_f32_e32 v62, v60, v62
	v_add_f32_e32 v63, v61, v63
	v_cvt_pk_bf16_f32 v52, v98, v99
	v_add_f32_e32 v62, v62, v63
	v_cvt_pk_bf16_f32 v56, v58, v59
	v_cvt_pk_bf16_f32 v53, v100, v101
	v_cvt_pk_bf16_f32 v57, v60, v61
	v_add_f32_e32 v139, v139, v62
	s_and_b64 vcc, exec, s[4:5]
	s_cbranch_vccz .LBB0_311

; __device__ __forceinline__ unsigned cvtpk(float lo, float hi) { f32x2_t v = {lo, hi}; bf16x2_t b = __builtin_convertvector(v, bf16x2_t); return __builtin_bit_cast(unsigned, b); }
; __device__ __forceinline__ s16x4 vtr(lds_cptr p) { return __builtin_bit_cast(s16x4, __builtin_amdgcn_ds_read_tr16_b64_v4i16((__attribute__((address_space(3))) v4i16_t*)p)); }
; template <class BIAS>
; __device__ __forceinline__ void attn_tiles(char* shm, const UnitIO& io, int t_begin, int t_end, const BIAS& B, int tid) {
;     ...
;         if (act) {
;             const lds_cptr vp = vp0 + sl_c;
;             s16x4 vlo[8], vhi[8];
; #pragma unroll
;             for (int i = 0; i < 8; ++i) { vlo[i] = vtr(vp + (i >> 2) * 4096 + (i & 3) * 1024); vhi[i] = vtr(vp + (i >> 2) * 4096 + (i & 3) * 1024 + 512); }
;             ATT_SBAR();
;             { float s1 = 0.f;
; #pragma unroll
;               for (int r = 0; r < 16; ++r) c1x[r] = __builtin_amdgcn_exp2f(c1x[r]);
;               { f32x2_t s2 = (f32x2_t){c1x[0], c1x[1]};
; #pragma unroll
;                 for (int i = 1; i < 8; ++i) s2 += (f32x2_t){c1x[2 * i], c1x[2 * i + 1]};
;                 s1 = s2[0] + s2[1]; }
;               l_reg += s1;
; #pragma unroll
;               for (int i = 0; i < 4; ++i) { pw[2][i] = cvtpk(c1x[2 * i], c1x[2 * i + 1]); pw[3][i] = cvtpk(c1x[8 + 2 * i], c1x[9 + 2 * i]); } }
;             ATT_SBAR();
;             asm volatile("" : "+v"(vlo[0]), "+v"(vhi[0]), "+v"(vlo[1]), "+v"(vhi[1]), "+v"(vlo[2]), "+v"(vhi[2]), "+v"(vlo[3]), "+v"(vhi[3]));
; #pragma unroll
;             for (int ks = 0; ks < 4; ++ks) { const bf16x8 vf = (bf16x8){vlo[ks][0], vlo[ks][1], vlo[ks][2], vlo[ks][3], vhi[ks][0], vhi[ks][1], vhi[ks][2], vhi[ks][3]};
;                 o[0] = __builtin_amdgcn_mfma_f32_32x32x16_bf16(__builtin_bit_cast(bf16x8, pw[ks]), vf, o[0], 0, 0, 0); }
;             ATT_SBAR();
;             asm volatile("" : "+v"(vlo[4]), "+v"(vhi[4]), "+v"(vlo[5]), "+v"(vhi[5]), "+v"(vlo[6]), "+v"(vhi[6]), "+v"(vlo[7]), "+v"(vhi[7]));
; #pragma unroll
;             for (int ks = 0; ks < 4; ++ks) { const bf16x8 vf = (bf16x8){vlo[4 + ks][0], vlo[4 + ks][1], vlo[4 + ks][2], vlo[4 + ks][3], vhi[4 + ks][0], vhi[4 + ks][1], vhi[4 + ks][2], vhi[4 + ks][3]};
;                 o[1] = __builtin_amdgcn_mfma_f32_32x32x16_bf16(__builtin_bit_cast(bf16x8, pw[ks]), vf, o[1], 0, 0, 0); }
;         }
.LBB0_311:
	v_add_u32_e32 v104, s23, v180
	ds_read_b64_tr_b16 v[58:59], v104 offset:32768
	ds_read_b64_tr_b16 v[60:61], v104 offset:33280
	ds_read_b64_tr_b16 v[62:63], v104 offset:33792
	ds_read_b64_tr_b16 v[64:65], v104 offset:34304
	ds_read_b64_tr_b16 v[82:83], v104 offset:34816
	ds_read_b64_tr_b16 v[84:85], v104 offset:35328
	ds_read_b64_tr_b16 v[86:87], v104 offset:35840
	ds_read_b64_tr_b16 v[88:89], v104 offset:36352
	ds_read_b64_tr_b16 v[90:91], v104 offset:36864
	ds_read_b64_tr_b16 v[92:93], v104 offset:37376
	ds_read_b64_tr_b16 v[94:95], v104 offset:37888
	ds_read_b64_tr_b16 v[96:97], v104 offset:38400
	ds_read_b64_tr_b16 v[98:99], v104 offset:38912
	ds_read_b64_tr_b16 v[100:101], v104 offset:39424
	ds_read_b64_tr_b16 v[102:103], v104 offset:39936
	ds_read_b64_tr_b16 v[104:105], v104 offset:40448
	v_exp_f32_e32 v34, v34
	v_exp_f32_e32 v35, v35
	v_exp_f32_e32 v36, v36
	v_exp_f32_e32 v37, v37
	s_waitcnt lgkmcnt(14)
	v_mfma_f32_32x32x16_bf16 v[2:17], v[50:53], v[58:61], v[2:17]
	v_exp_f32_e32 v38, v38
	v_exp_f32_e32 v39, v39
	v_exp_f32_e32 v40, v40
	v_exp_f32_e32 v41, v41
	s_waitcnt lgkmcnt(12)
	v_mfma_f32_32x32x16_bf16 v[2:17], v[54:57], v[62:65], v[2:17]
	v_exp_f32_e32 v42, v42
	v_exp_f32_e32 v43, v43
	v_exp_f32_e32 v44, v44
	v_exp_f32_e32 v45, v45
	s_waitcnt lgkmcnt(6)
	v_mfma_f32_32x32x16_bf16 v[18:33], v[50:53], v[90:93], v[18:33]
	v_add_f32_e32 v106, v36, v34
	v_add_f32_e32 v107, v37, v35
	v_exp_f32_e32 v46, v46
	v_exp_f32_e32 v47, v47
	s_waitcnt lgkmcnt(4)
	v_mfma_f32_32x32x16_bf16 v[18:33], v[54:57], v[94:97], v[18:33]
	v_add_f32_e32 v106, v38, v106
	v_add_f32_e32 v107, v39, v107
	v_exp_f32_e32 v48, v48
	v_exp_f32_e32 v49, v49
	v_add_f32_e32 v106, v40, v106
	v_add_f32_e32 v107, v41, v107
	v_cvt_pk_bf16_f32 v110, v42, v43
	v_add_f32_e32 v106, v42, v106
	v_add_f32_e32 v107, v43, v107
	v_cvt_pk_bf16_f32 v111, v44, v45
	v_add_f32_e32 v106, v44, v106
	v_add_f32_e32 v107, v45, v107
	v_cvt_pk_bf16_f32 v108, v38, v39
	v_add_f32_e32 v106, v46, v106
	v_add_f32_e32 v107, v47, v107
	v_cvt_pk_bf16_f32 v112, v46, v47
	v_add_f32_e32 v106, v48, v106
	v_add_f32_e32 v107, v49, v107
	v_cvt_pk_bf16_f32 v109, v40, v41
	v_add_f32_e32 v117, v106, v107
	v_cvt_pk_bf16_f32 v106, v34, v35
	v_cvt_pk_bf16_f32 v107, v36, v37
	v_cvt_pk_bf16_f32 v113, v48, v49
	s_waitcnt lgkmcnt(0)
	s_nop 0
	v_mfma_f32_32x32x16_bf16 v[2:17], v[106:109], v[82:85], v[2:17]
	v_mfma_f32_32x32x16_bf16 v[2:17], v[110:113], v[86:89], v[2:17]
	v_add_f32_e32 v139, v139, v117
	v_mfma_f32_32x32x16_bf16 v[18:33], v[106:109], v[98:101], v[18:33]
	v_mfma_f32_32x32x16_bf16 v[18:33], v[110:113], v[102:105], v[18:33]
	s_mov_b64 s[4:5], -1
	s_and_b64 vcc, exec, s[12:13]
	s_cbranch_vccnz .LBB0_305

; __device__ __forceinline__ unsigned cvtpk(float lo, float hi) { f32x2_t v = {lo, hi}; bf16x2_t b = __builtin_convertvector(v, bf16x2_t); return __builtin_bit_cast(unsigned, b); }
; template <class BIAS>
; __device__ __forceinline__ void attn_tiles(char* shm, const UnitIO& io, int t_begin, int t_end, const BIAS& B, int tid) {
;     ...
;             for (int d0 = 0; d0 < 4; ++d0) { c0 = __builtin_amdgcn_mfma_f32_32x32x16_bf16(kf[2 * d0], qr[d0], c0, 0, 0, 0); c1 = __builtin_amdgcn_mfma_f32_32x32x16_bf16(kf[2 * d0 + 1], qr[d0], c1, 0, 0, 0); }
;             float s0 = 0.f;
; #pragma unroll
;             for (int r = 0; r < 16; ++r) c0[r] = __builtin_amdgcn_exp2f(c0[r]);
;             { f32x2_t s2 = (f32x2_t){c0[0], c0[1]};
; #pragma unroll
;               for (int i = 1; i < 8; ++i) s2 += (f32x2_t){c0[2 * i], c0[2 * i + 1]};
;               s0 = s2[0] + s2[1]; }
;             l_reg += s0;
; #pragma unroll
;             for (int i = 0; i < 4; ++i) { pw[0][i] = cvtpk(c0[2 * i], c0[2 * i + 1]); pw[1][i] = cvtpk(c0[8 + 2 * i], c0[9 + 2 * i]); }
;             c1x = c1;
.LBB0_347:
	s_nop 1
	v_mfma_f32_32x32x16_bf16 v[66:81], v[114:117], v[82:85], v[66:81]
	v_mfma_f32_32x32x16_bf16 v[66:81], v[118:121], v[86:89], v[66:81]
	v_mfma_f32_32x32x16_bf16 v[66:81], v[122:125], v[90:93], v[66:81]
	v_mfma_f32_32x32x16_bf16 v[66:81], v[126:129], v[94:97], v[66:81]
	v_mfma_f32_32x32x16_bf16 v[50:65], v[110:113], v[82:85], v[50:65]
	s_nop 10
	v_exp_f32_e32 v66, v66
	v_exp_f32_e32 v67, v67
	v_exp_f32_e32 v68, v68
	v_exp_f32_e32 v69, v69
	v_mfma_f32_32x32x16_bf16 v[50:65], v[106:109], v[86:89], v[50:65]
	v_exp_f32_e32 v114, v70
	v_exp_f32_e32 v115, v71
	v_exp_f32_e32 v116, v72
	v_exp_f32_e32 v117, v73
	v_mfma_f32_32x32x16_bf16 v[50:65], v[102:105], v[90:93], v[50:65]
	v_exp_f32_e32 v70, v74
	v_exp_f32_e32 v71, v75
	v_exp_f32_e32 v72, v76
	v_exp_f32_e32 v73, v77
	v_mfma_f32_32x32x16_bf16 v[50:65], v[98:101], v[94:97], v[50:65]
	v_exp_f32_e32 v74, v78
	v_exp_f32_e32 v75, v79
	v_add_f32_e32 v78, v66, v68
	v_add_f32_e32 v79, v67, v69
	v_add_f32_e64 v78, v114, v78
	v_add_f32_e64 v79, v115, v79
	v_exp_f32_e32 v76, v80
	v_exp_f32_e32 v77, v81
	v_add_f32_e32 v78, v116, v78
	v_add_f32_e32 v79, v117, v79
	v_cvt_pk_bf16_f32 v66, v66, v67
	v_add_f32_e32 v78, v70, v78
	v_add_f32_e32 v79, v71, v79
	v_cvt_pk_bf16_f32 v70, v70, v71
	v_add_f32_e32 v78, v72, v78
	v_add_f32_e32 v79, v73, v79
	v_cvt_pk_bf16_f32 v67, v68, v69
	v_add_f32_e32 v78, v74, v78
	v_add_f32_e32 v79, v75, v79
	v_cvt_pk_bf16_f32 v71, v72, v73
	v_add_f32_e32 v78, v76, v78
	v_add_f32_e32 v79, v77, v79
	v_cvt_pk_bf16_f32 v68, v114, v115
	v_add_f32_e32 v78, v78, v79
	v_cvt_pk_bf16_f32 v72, v74, v75
	v_cvt_pk_bf16_f32 v69, v116, v117
	v_cvt_pk_bf16_f32 v73, v76, v77
	v_add_f32_e32 v135, v135, v78
	s_and_b64 vcc, exec, s[34:35]
	s_cbranch_vccz .LBB0_355

; __device__ __forceinline__ unsigned cvtpk(float lo, float hi) { f32x2_t v = {lo, hi}; bf16x2_t b = __builtin_convertvector(v, bf16x2_t); return __builtin_bit_cast(unsigned, b); }
; __device__ __forceinline__ s16x4 vtr(lds_cptr p) { return __builtin_bit_cast(s16x4, __builtin_amdgcn_ds_read_tr16_b64_v4i16((__attribute__((address_space(3))) v4i16_t*)p)); }
; template <class BIAS>
; __device__ __forceinline__ void attn_tiles(char* shm, const UnitIO& io, int t_begin, int t_end, const BIAS& B, int tid) {
;     ...
;         if (act) {
;             const lds_cptr vp = vp0 + sl_c;
;             s16x4 vlo[8], vhi[8];
; #pragma unroll
;             for (int i = 0; i < 8; ++i) { vlo[i] = vtr(vp + (i >> 2) * 4096 + (i & 3) * 1024); vhi[i] = vtr(vp + (i >> 2) * 4096 + (i & 3) * 1024 + 512); }
;             ATT_SBAR();
;             { float s1 = 0.f;
; #pragma unroll
;               for (int r = 0; r < 16; ++r) c1x[r] = __builtin_amdgcn_exp2f(c1x[r]);
;               { f32x2_t s2 = (f32x2_t){c1x[0], c1x[1]};
; #pragma unroll
;                 for (int i = 1; i < 8; ++i) s2 += (f32x2_t){c1x[2 * i], c1x[2 * i + 1]};
;                 s1 = s2[0] + s2[1]; }
;               l_reg += s1;
; #pragma unroll
;               for (int i = 0; i < 4; ++i) { pw[2][i] = cvtpk(c1x[2 * i], c1x[2 * i + 1]); pw[3][i] = cvtpk(c1x[8 + 2 * i], c1x[9 + 2 * i]); } }
;             ATT_SBAR();
;             asm volatile("" : "+v"(vlo[0]), "+v"(vhi[0]), "+v"(vlo[1]), "+v"(vhi[1]), "+v"(vlo[2]), "+v"(vhi[2]), "+v"(vlo[3]), "+v"(vhi[3]));
; #pragma unroll
;             for (int ks = 0; ks < 4; ++ks) { const bf16x8 vf = (bf16x8){vlo[ks][0], vlo[ks][1], vlo[ks][2], vlo[ks][3], vhi[ks][0], vhi[ks][1], vhi[ks][2], vhi[ks][3]};
;                 o[0] = __builtin_amdgcn_mfma_f32_32x32x16_bf16(__builtin_bit_cast(bf16x8, pw[ks]), vf, o[0], 0, 0, 0); }
;             ATT_SBAR();
;             asm volatile("" : "+v"(vlo[4]), "+v"(vhi[4]), "+v"(vlo[5]), "+v"(vhi[5]), "+v"(vlo[6]), "+v"(vhi[6]), "+v"(vlo[7]), "+v"(vhi[7]));
; #pragma unroll
;             for (int ks = 0; ks < 4; ++ks) { const bf16x8 vf = (bf16x8){vlo[4 + ks][0], vlo[4 + ks][1], vlo[4 + ks][2], vlo[4 + ks][3], vhi[4 + ks][0], vhi[4 + ks][1], vhi[4 + ks][2], vhi[4 + ks][3]};
;                 o[1] = __builtin_amdgcn_mfma_f32_32x32x16_bf16(__builtin_bit_cast(bf16x8, pw[ks]), vf, o[1], 0, 0, 0); }
;         }
.LBB0_355:
	v_add_u32_e32 v120, s20, v180
	ds_read_b64_tr_b16 v[74:75], v120 offset:32768
	ds_read_b64_tr_b16 v[76:77], v120 offset:33280
	ds_read_b64_tr_b16 v[78:79], v120 offset:33792
	ds_read_b64_tr_b16 v[80:81], v120 offset:34304
	ds_read_b64_tr_b16 v[98:99], v120 offset:34816
	ds_read_b64_tr_b16 v[100:101], v120 offset:35328
	ds_read_b64_tr_b16 v[102:103], v120 offset:35840
	ds_read_b64_tr_b16 v[104:105], v120 offset:36352
	ds_read_b64_tr_b16 v[106:107], v120 offset:36864
	ds_read_b64_tr_b16 v[108:109], v120 offset:37376
	ds_read_b64_tr_b16 v[110:111], v120 offset:37888
	ds_read_b64_tr_b16 v[112:113], v120 offset:38400
	ds_read_b64_tr_b16 v[114:115], v120 offset:38912
	ds_read_b64_tr_b16 v[116:117], v120 offset:39424
	ds_read_b64_tr_b16 v[118:119], v120 offset:39936
	ds_read_b64_tr_b16 v[120:121], v120 offset:40448
	v_exp_f32_e32 v50, v50
	v_exp_f32_e32 v51, v51
	v_exp_f32_e32 v52, v52
	v_exp_f32_e32 v53, v53
	s_waitcnt lgkmcnt(14)
	v_mfma_f32_32x32x16_bf16 v[12:27], v[66:69], v[74:77], v[12:27]
	v_exp_f32_e32 v54, v54
	v_exp_f32_e32 v55, v55
	v_exp_f32_e32 v56, v56
	v_exp_f32_e32 v57, v57
	s_waitcnt lgkmcnt(12)
	v_mfma_f32_32x32x16_bf16 v[12:27], v[70:73], v[78:81], v[12:27]
	v_exp_f32_e32 v58, v58
	v_exp_f32_e32 v59, v59
	v_exp_f32_e32 v60, v60
	v_exp_f32_e32 v61, v61
	s_waitcnt lgkmcnt(6)
	v_mfma_f32_32x32x16_bf16 v[34:49], v[66:69], v[106:109], v[34:49]
	v_add_f32_e32 v122, v52, v50
	v_add_f32_e32 v123, v53, v51
	v_exp_f32_e32 v62, v62
	v_exp_f32_e32 v63, v63
	s_waitcnt lgkmcnt(4)
	v_mfma_f32_32x32x16_bf16 v[34:49], v[70:73], v[110:113], v[34:49]
	v_add_f32_e32 v122, v54, v122
	v_add_f32_e32 v123, v55, v123
	v_exp_f32_e32 v64, v64
	v_exp_f32_e32 v65, v65
	v_add_f32_e32 v122, v56, v122
	v_add_f32_e32 v123, v57, v123
	v_cvt_pk_bf16_f32 v126, v58, v59
	v_add_f32_e32 v122, v58, v122
	v_add_f32_e32 v123, v59, v123
	v_cvt_pk_bf16_f32 v127, v60, v61
	v_add_f32_e32 v122, v60, v122
	v_add_f32_e32 v123, v61, v123
	v_cvt_pk_bf16_f32 v124, v54, v55
	v_add_f32_e32 v122, v62, v122
	v_add_f32_e32 v123, v63, v123
	v_cvt_pk_bf16_f32 v128, v62, v63
	v_add_f32_e32 v122, v64, v122
	v_add_f32_e32 v123, v65, v123
	v_cvt_pk_bf16_f32 v125, v56, v57
	v_add_f32_e32 v139, v122, v123
	v_cvt_pk_bf16_f32 v122, v50, v51
	v_cvt_pk_bf16_f32 v123, v52, v53
	v_cvt_pk_bf16_f32 v129, v64, v65
	s_waitcnt lgkmcnt(0)
	s_nop 0
	v_mfma_f32_32x32x16_bf16 v[12:27], v[122:125], v[98:101], v[12:27]
	v_mfma_f32_32x32x16_bf16 v[12:27], v[126:129], v[102:105], v[12:27]
	v_add_f32_e32 v135, v135, v139
	v_mfma_f32_32x32x16_bf16 v[34:49], v[122:125], v[114:117], v[34:49]
	v_mfma_f32_32x32x16_bf16 v[34:49], v[126:129], v[118:121], v[34:49]
	s_mov_b64 s[34:35], -1
	s_and_b64 vcc, exec, s[46:47]
	s_cbranch_vccnz .LBB0_349

; __device__ __forceinline__ unsigned cvtpk(float lo, float hi) { f32x2_t v = {lo, hi}; bf16x2_t b = __builtin_convertvector(v, bf16x2_t); return __builtin_bit_cast(unsigned, b); }
; __device__ __forceinline__ s16x4 vtr(lds_cptr p) { return __builtin_bit_cast(s16x4, __builtin_amdgcn_ds_read_tr16_b64_v4i16((__attribute__((address_space(3))) v4i16_t*)p)); }
; template <class BIAS>
; __device__ __forceinline__ void attn_tiles(char* shm, const UnitIO& io, int t_begin, int t_end, const BIAS& B, int tid) {
;     ...
;         if (act) {
;             const lds_cptr vp = vp0 + sl_c;
;             s16x4 vlo[8], vhi[8];
; #pragma unroll
;             for (int i = 0; i < 8; ++i) { vlo[i] = vtr(vp + (i >> 2) * 4096 + (i & 3) * 1024); vhi[i] = vtr(vp + (i >> 2) * 4096 + (i & 3) * 1024 + 512); }
;             ATT_SBAR();
;             { float s1 = 0.f;
; #pragma unroll
;               for (int r = 0; r < 16; ++r) c1x[r] = __builtin_amdgcn_exp2f(c1x[r]);
;               { f32x2_t s2 = (f32x2_t){c1x[0], c1x[1]};
; #pragma unroll
;                 for (int i = 1; i < 8; ++i) s2 += (f32x2_t){c1x[2 * i], c1x[2 * i + 1]};
;                 s1 = s2[0] + s2[1]; }
;               l_reg += s1;
; #pragma unroll
;               for (int i = 0; i < 4; ++i) { pw[2][i] = cvtpk(c1x[2 * i], c1x[2 * i + 1]); pw[3][i] = cvtpk(c1x[8 + 2 * i], c1x[9 + 2 * i]); } }
;             ATT_SBAR();
;             asm volatile("" : "+v"(vlo[0]), "+v"(vhi[0]), "+v"(vlo[1]), "+v"(vhi[1]), "+v"(vlo[2]), "+v"(vhi[2]), "+v"(vlo[3]), "+v"(vhi[3]));
; #pragma unroll
;             for (int ks = 0; ks < 4; ++ks) { const bf16x8 vf = (bf16x8){vlo[ks][0], vlo[ks][1], vlo[ks][2], vlo[ks][3], vhi[ks][0], vhi[ks][1], vhi[ks][2], vhi[ks][3]};
;                 o[0] = __builtin_amdgcn_mfma_f32_32x32x16_bf16(__builtin_bit_cast(bf16x8, pw[ks]), vf, o[0], 0, 0, 0); }
;             ATT_SBAR();
;             asm volatile("" : "+v"(vlo[4]), "+v"(vhi[4]), "+v"(vlo[5]), "+v"(vhi[5]), "+v"(vlo[6]), "+v"(vhi[6]), "+v"(vlo[7]), "+v"(vhi[7]));
; #pragma unroll
;             for (int ks = 0; ks < 4; ++ks) { const bf16x8 vf = (bf16x8){vlo[4 + ks][0], vlo[4 + ks][1], vlo[4 + ks][2], vlo[4 + ks][3], vhi[4 + ks][0], vhi[4 + ks][1], vhi[4 + ks][2], vhi[4 + ks][3]};
;                 o[1] = __builtin_amdgcn_mfma_f32_32x32x16_bf16(__builtin_bit_cast(bf16x8, pw[ks]), vf, o[1], 0, 0, 0); }
;         }
.LBB0_375:
	v_add_u32_e32 v88, s82, v180
	ds_read_b64_tr_b16 v[58:59], v88 offset:32768
	ds_read_b64_tr_b16 v[60:61], v88 offset:33280
	ds_read_b64_tr_b16 v[62:63], v88 offset:33792
	ds_read_b64_tr_b16 v[64:65], v88 offset:34304
	ds_read_b64_tr_b16 v[66:67], v88 offset:34816
	ds_read_b64_tr_b16 v[68:69], v88 offset:35328
	ds_read_b64_tr_b16 v[70:71], v88 offset:35840
	ds_read_b64_tr_b16 v[72:73], v88 offset:36352
	ds_read_b64_tr_b16 v[74:75], v88 offset:36864
	ds_read_b64_tr_b16 v[76:77], v88 offset:37376
	ds_read_b64_tr_b16 v[78:79], v88 offset:37888
	ds_read_b64_tr_b16 v[80:81], v88 offset:38400
	ds_read_b64_tr_b16 v[82:83], v88 offset:38912
	ds_read_b64_tr_b16 v[84:85], v88 offset:39424
	ds_read_b64_tr_b16 v[86:87], v88 offset:39936
	ds_read_b64_tr_b16 v[88:89], v88 offset:40448
	v_exp_f32_e32 v34, v34
	v_exp_f32_e32 v35, v35
	v_exp_f32_e32 v36, v36
	v_exp_f32_e32 v37, v37
	s_waitcnt lgkmcnt(14)
	v_mfma_f32_32x32x16_bf16 v[2:17], v[50:53], v[58:61], v[2:17]
	v_exp_f32_e32 v38, v38
	v_exp_f32_e32 v39, v39
	v_exp_f32_e32 v40, v40
	v_exp_f32_e32 v41, v41
	s_waitcnt lgkmcnt(12)
	v_mfma_f32_32x32x16_bf16 v[2:17], v[54:57], v[62:65], v[2:17]
	v_exp_f32_e32 v42, v42
	v_exp_f32_e32 v43, v43
	v_exp_f32_e32 v44, v44
	v_exp_f32_e32 v45, v45
	s_waitcnt lgkmcnt(6)
	v_mfma_f32_32x32x16_bf16 v[18:33], v[50:53], v[74:77], v[18:33]
	v_add_f32_e32 v90, v36, v34
	v_add_f32_e32 v91, v37, v35
	v_exp_f32_e32 v46, v46
	v_exp_f32_e32 v47, v47
	s_waitcnt lgkmcnt(4)
	v_mfma_f32_32x32x16_bf16 v[18:33], v[54:57], v[78:81], v[18:33]
	v_add_f32_e32 v90, v38, v90
	v_add_f32_e32 v91, v39, v91
	v_exp_f32_e32 v48, v48
	v_exp_f32_e32 v49, v49
	v_add_f32_e32 v90, v40, v90
	v_add_f32_e32 v91, v41, v91
	v_cvt_pk_bf16_f32 v94, v42, v43
	v_add_f32_e32 v90, v42, v90
	v_add_f32_e32 v91, v43, v91
	v_cvt_pk_bf16_f32 v95, v44, v45
	v_add_f32_e32 v90, v44, v90
	v_add_f32_e32 v91, v45, v91
	v_cvt_pk_bf16_f32 v92, v38, v39
	v_add_f32_e32 v90, v46, v90
	v_add_f32_e32 v91, v47, v91
	v_cvt_pk_bf16_f32 v96, v46, v47
	v_add_f32_e32 v90, v48, v90
	v_add_f32_e32 v91, v49, v91
	v_cvt_pk_bf16_f32 v93, v40, v41
	v_add_f32_e32 v114, v90, v91
	v_cvt_pk_bf16_f32 v90, v34, v35
	v_cvt_pk_bf16_f32 v91, v36, v37
	v_cvt_pk_bf16_f32 v97, v48, v49
	s_waitcnt lgkmcnt(0)
	s_nop 0
	v_mfma_f32_32x32x16_bf16 v[2:17], v[90:93], v[66:69], v[2:17]
	v_mfma_f32_32x32x16_bf16 v[2:17], v[94:97], v[70:73], v[2:17]
	v_add_f32_e32 v151, v151, v114
	v_mfma_f32_32x32x16_bf16 v[18:33], v[90:93], v[82:85], v[18:33]
	v_mfma_f32_32x32x16_bf16 v[18:33], v[94:97], v[86:89], v[18:33]
	s_mov_b64 s[56:57], -1
	s_and_b64 vcc, exec, s[68:69]
	s_cbranch_vccnz .LBB0_382

; __device__ __forceinline__ unsigned cvtpk(float lo, float hi) { f32x2_t v = {lo, hi}; bf16x2_t b = __builtin_convertvector(v, bf16x2_t); return __builtin_bit_cast(unsigned, b); }
; template <class BIAS>
; __device__ __forceinline__ void attn_tiles(char* shm, const UnitIO& io, int t_begin, int t_end, const BIAS& B, int tid) {
;     ...
;             for (int d0 = 0; d0 < 4; ++d0) { c0 = __builtin_amdgcn_mfma_f32_32x32x16_bf16(kf[2 * d0], qr[d0], c0, 0, 0, 0); c1 = __builtin_amdgcn_mfma_f32_32x32x16_bf16(kf[2 * d0 + 1], qr[d0], c1, 0, 0, 0); }
;             float s0 = 0.f;
; #pragma unroll
;             for (int r = 0; r < 16; ++r) c0[r] = __builtin_amdgcn_exp2f(c0[r]);
;             { f32x2_t s2 = (f32x2_t){c0[0], c0[1]};
; #pragma unroll
;               for (int i = 1; i < 8; ++i) s2 += (f32x2_t){c0[2 * i], c0[2 * i + 1]};
;               s0 = s2[0] + s2[1]; }
;             l_reg += s0;
; #pragma unroll
;             for (int i = 0; i < 4; ++i) { pw[0][i] = cvtpk(c0[2 * i], c0[2 * i + 1]); pw[1][i] = cvtpk(c0[8 + 2 * i], c0[9 + 2 * i]); }
;             c1x = c1;
.Ldil_h1_go:
	s_waitcnt lgkmcnt(0)
	s_nop 0
	v_mfma_f32_32x32x16_bf16 v[82:97], v[130:133], v[98:101], v[82:97]
	v_mfma_f32_32x32x16_bf16 v[82:97], v[134:137], v[102:105], v[82:97]
	v_mfma_f32_32x32x16_bf16 v[82:97], v[138:141], v[106:109], v[82:97]
	v_mfma_f32_32x32x16_bf16 v[82:97], v[142:145], v[110:113], v[82:97]
	v_mfma_f32_32x32x16_bf16 v[34:49], v[126:129], v[98:101], v[34:49]
	s_nop 10
	v_exp_f32_e32 v50, v82
	v_exp_f32_e32 v51, v83
	v_exp_f32_e32 v52, v84
	v_exp_f32_e32 v53, v85
	v_mfma_f32_32x32x16_bf16 v[34:49], v[122:125], v[102:105], v[34:49]
	v_exp_f32_e32 v56, v86
	v_exp_f32_e32 v57, v87
	v_exp_f32_e32 v58, v88
	v_exp_f32_e32 v59, v89
	v_mfma_f32_32x32x16_bf16 v[34:49], v[118:121], v[106:109], v[34:49]
	v_exp_f32_e32 v54, v90
	v_exp_f32_e32 v55, v91
	v_exp_f32_e32 v60, v92
	v_exp_f32_e32 v61, v93
	v_mfma_f32_32x32x16_bf16 v[34:49], v[114:117], v[110:113], v[34:49]
	v_add_f32_e32 v66, v50, v52
	v_add_f32_e32 v67, v51, v53
	v_exp_f32_e32 v62, v94
	v_exp_f32_e32 v63, v95
	v_add_f32_e32 v66, v56, v66
	v_add_f32_e32 v67, v57, v67
	v_exp_f32_e32 v64, v96
	v_exp_f32_e32 v65, v97
	v_add_f32_e32 v66, v58, v66
	v_add_f32_e32 v67, v59, v67
	v_cvt_pk_bf16_f32 v50, v50, v51
	v_add_f32_e32 v66, v54, v66
	v_add_f32_e32 v67, v55, v67
	v_cvt_pk_bf16_f32 v54, v54, v55
	v_add_f32_e32 v66, v60, v66
	v_add_f32_e32 v67, v61, v67
	v_cvt_pk_bf16_f32 v51, v52, v53
	v_add_f32_e32 v66, v62, v66
	v_add_f32_e32 v67, v63, v67
	v_cvt_pk_bf16_f32 v55, v60, v61
	v_add_f32_e32 v66, v64, v66
	v_add_f32_e32 v67, v65, v67
	v_cvt_pk_bf16_f32 v52, v56, v57
	v_add_f32_e32 v66, v66, v67
	v_cvt_pk_bf16_f32 v56, v62, v63
	v_cvt_pk_bf16_f32 v53, v58, v59
	v_cvt_pk_bf16_f32 v57, v64, v65
	v_add_f32_e32 v151, v151, v66
	s_and_b64 vcc, exec, s[56:57]
	s_cbranch_vccz .LBB0_375
